# V loop first half: 15 of the 16 s_nop placeholders left by the removed wait ladder deleted (the remaining one supplies a VALU->MFMA wait state)
# speedup vs baseline: 1.0158x; 1.0010x over previous
.Lpv_skip1:
	s_lshl_b32 s30, s56, 4
	s_cmp_ge_i32 s30, s60
	s_cselect_b64 s[38:39], -1, 0
	s_cmp_lt_i32 s30, s48
	s_cselect_b64 s[52:53], -1, 0
	s_waitcnt lgkmcnt(0)
	v_mul_f32_e32 v1, 0x45000000, v170
	s_and_b64 vcc, s[38:39], s[52:53]
	v_cndmask_b32_e32 v1, 0, v1, vcc
	v_mov_b32_e32 v2, v0
	s_or_b32 s52, s30, 1
	v_cvt_pk_fp8_f32 v2, v1, v1
	s_cmp_ge_i32 s52, s60
	s_cselect_b64 s[38:39], -1, 0
	s_cmp_lt_i32 s52, s48
	s_cselect_b64 s[52:53], -1, 0
	v_mul_f32_e32 v169, 0x45000000, v171
	s_and_b64 vcc, s[38:39], s[52:53]
	v_cvt_pk_fp8_f32 v2, v1, v1 op_sel:[0,0,1]
	v_cndmask_b32_e32 v169, 0, v169, vcc
	v_mov_b32_e32 v170, v0
	v_cvt_pk_fp8_f32 v170, v169, v169
	v_mov_b32_e32 v3, v0
	v_and_b32_e32 v2, v2, v249
	s_or_b32 s52, s30, 2
	v_cvt_pk_fp8_f32 v170, v169, v169 op_sel:[0,0,1]
	s_cmp_ge_i32 s52, s60
	s_cselect_b64 s[38:39], -1, 0
	s_cmp_lt_i32 s52, s48
	s_cselect_b64 s[52:53], -1, 0
	v_mul_f32_e32 v169, 0x45000000, v172
	s_and_b64 vcc, s[38:39], s[52:53]
	v_mov_b32_e32 v1, v2
	v_mfma_f32_16x16x32_fp8_fp8 v[160:163], v[2:3], v[68:69], v[160:163]
	v_cndmask_b32_e32 v169, 0, v169, vcc
	s_or_b32 s52, s30, 3
	s_cmp_ge_i32 s52, s60
	v_mfma_f32_16x16x32_fp8_fp8 v[152:155], v[2:3], v[70:71], v[152:155]
	v_and_b32_e32 v2, v170, v249
	v_mov_b32_e32 v170, v0
	v_cvt_pk_fp8_f32 v170, v169, v169
	v_mfma_f32_16x16x32_fp8_fp8 v[164:167], v[0:1], v[68:69], v[164:167]
	s_cselect_b64 s[38:39], -1, 0
	s_cmp_lt_i32 s52, s48
	v_cvt_pk_fp8_f32 v170, v169, v169 op_sel:[0,0,1]
	v_mfma_f32_16x16x32_fp8_fp8 v[156:159], v[0:1], v[70:71], v[156:159]
	v_mov_b32_e32 v1, v2
	s_cselect_b64 s[52:53], -1, 0
	s_and_b64 vcc, s[38:39], s[52:53]
	v_mfma_f32_16x16x32_fp8_fp8 v[160:163], v[2:3], v[72:73], v[160:163]
	s_or_b32 s52, s30, 4
	s_cmp_ge_i32 s52, s60
	s_cselect_b64 s[38:39], -1, 0
	v_mfma_f32_16x16x32_fp8_fp8 v[152:155], v[2:3], v[74:75], v[152:155]
	v_and_b32_e32 v2, v170, v249
	v_mov_b32_e32 v170, v0
	s_cmp_lt_i32 s52, s48
	v_mfma_f32_16x16x32_fp8_fp8 v[184:187], v[2:3], v[76:77], v[160:163]
	s_cselect_b64 s[52:53], -1, 0
	s_nop 1
	v_mul_f32_e32 v160, 0x45000000, v173
	v_cndmask_b32_e32 v169, 0, v160, vcc
	v_cvt_pk_fp8_f32 v170, v169, v169
	v_mfma_f32_16x16x32_fp8_fp8 v[164:167], v[0:1], v[72:73], v[164:167]
	s_and_b64 vcc, s[38:39], s[52:53]
	s_or_b32 s52, s30, 5
	v_cvt_pk_fp8_f32 v170, v169, v169 op_sel:[0,0,1]
	v_mfma_f32_16x16x32_fp8_fp8 v[156:159], v[0:1], v[74:75], v[156:159]
	v_mov_b32_e32 v1, v2
	s_cmp_ge_i32 s52, s60
	s_cselect_b64 s[38:39], -1, 0
	v_mfma_f32_16x16x32_fp8_fp8 v[160:163], v[2:3], v[78:79], v[152:155]
	v_and_b32_e32 v2, v170, v249
	ds_read_b128 v[170:173], v168 offset:16
	s_cmp_lt_i32 s52, s48
	s_cselect_b64 s[52:53], -1, 0
	v_mfma_f32_16x16x32_fp8_fp8 v[164:167], v[0:1], v[76:77], v[164:167]
	s_waitcnt lgkmcnt(0)
	v_mul_f32_e32 v169, 0x45000000, v170
	v_cndmask_b32_e32 v169, 0, v169, vcc
	v_mov_b32_e32 v170, v0
	v_cvt_pk_fp8_f32 v170, v169, v169
	s_and_b64 vcc, s[38:39], s[52:53]
	v_mfma_f32_16x16x32_fp8_fp8 v[156:159], v[0:1], v[78:79], v[156:159]
	v_mov_b32_e32 v1, v2
	v_cvt_pk_fp8_f32 v170, v169, v169 op_sel:[0,0,1]
	v_mul_f32_e32 v169, 0x45000000, v171
	v_mfma_f32_16x16x32_fp8_fp8 v[152:155], v[2:3], v[80:81], v[184:187]
	v_cndmask_b32_e32 v169, 0, v169, vcc
	s_or_b32 s52, s30, 6
	s_cmp_ge_i32 s52, s60
	v_mfma_f32_16x16x32_fp8_fp8 v[160:163], v[2:3], v[82:83], v[160:163]
	v_and_b32_e32 v2, v170, v249
	v_mov_b32_e32 v170, v0
	v_cvt_pk_fp8_f32 v170, v169, v169
	s_cselect_b64 s[38:39], -1, 0
	s_cmp_lt_i32 s52, s48
	s_cselect_b64 s[52:53], -1, 0
	v_cvt_pk_fp8_f32 v170, v169, v169 op_sel:[0,0,1]
	v_mul_f32_e32 v169, 0x45000000, v172
	s_and_b64 vcc, s[38:39], s[52:53]
	v_mfma_f32_16x16x32_fp8_fp8 v[164:167], v[0:1], v[80:81], v[164:167]
	v_cndmask_b32_e32 v169, 0, v169, vcc
	s_or_b32 s52, s30, 7
	s_cmp_ge_i32 s52, s60
	v_mfma_f32_16x16x32_fp8_fp8 v[156:159], v[0:1], v[82:83], v[156:159]
	v_mov_b32_e32 v1, v2
	s_cselect_b64 s[38:39], -1, 0
	s_cmp_lt_i32 s52, s48
	v_mfma_f32_16x16x32_fp8_fp8 v[152:155], v[2:3], v[84:85], v[152:155]
	s_cselect_b64 s[52:53], -1, 0
	s_and_b64 vcc, s[38:39], s[52:53]
	s_or_b32 s52, s30, 8
	v_mfma_f32_16x16x32_fp8_fp8 v[160:163], v[2:3], v[86:87], v[160:163]
	v_and_b32_e32 v2, v170, v249
	v_mov_b32_e32 v170, v0
	v_cvt_pk_fp8_f32 v170, v169, v169
	v_mfma_f32_16x16x32_fp8_fp8 v[164:167], v[0:1], v[84:85], v[164:167]
	s_cmp_ge_i32 s52, s60
	s_cselect_b64 s[38:39], -1, 0
	v_cvt_pk_fp8_f32 v170, v169, v169 op_sel:[0,0,1]
	v_mul_f32_e32 v169, 0x45000000, v173
	v_mfma_f32_16x16x32_fp8_fp8 v[156:159], v[0:1], v[86:87], v[156:159]
	v_mov_b32_e32 v1, v2
	v_cndmask_b32_e32 v169, 0, v169, vcc
	s_cmp_lt_i32 s52, s48
	v_mfma_f32_16x16x32_fp8_fp8 v[152:155], v[2:3], v[88:89], v[152:155]
	s_cselect_b64 s[52:53], -1, 0
	s_and_b64 vcc, s[38:39], s[52:53]
	s_or_b32 s52, s30, 9
	v_mfma_f32_16x16x32_fp8_fp8 v[160:163], v[2:3], v[90:91], v[160:163]
	v_and_b32_e32 v2, v170, v249
	v_mov_b32_e32 v170, v0
	v_cvt_pk_fp8_f32 v170, v169, v169
	v_mfma_f32_16x16x32_fp8_fp8 v[164:167], v[0:1], v[88:89], v[164:167]
	s_cmp_ge_i32 s52, s60
	s_cselect_b64 s[38:39], -1, 0
	v_cvt_pk_fp8_f32 v170, v169, v169 op_sel:[0,0,1]
	v_mfma_f32_16x16x32_fp8_fp8 v[156:159], v[0:1], v[90:91], v[156:159]
	v_mov_b32_e32 v1, v2
	s_cmp_lt_i32 s52, s48
	s_cselect_b64 s[52:53], -1, 0
	v_mfma_f32_16x16x32_fp8_fp8 v[152:155], v[2:3], v[92:93], v[152:155]
	v_mfma_f32_16x16x32_fp8_fp8 v[160:163], v[2:3], v[94:95], v[160:163]
	v_and_b32_e32 v2, v170, v249
	ds_read_b128 v[170:173], v168 offset:32
	s_waitcnt lgkmcnt(0)
	v_mul_f32_e32 v169, 0x45000000, v170
	v_cndmask_b32_e32 v169, 0, v169, vcc
	v_mov_b32_e32 v170, v0
	v_cvt_pk_fp8_f32 v170, v169, v169
	s_and_b64 vcc, s[38:39], s[52:53]
	v_mfma_f32_16x16x32_fp8_fp8 v[164:167], v[0:1], v[92:93], v[164:167]
	s_or_b32 s52, s30, 10
	v_cvt_pk_fp8_f32 v170, v169, v169 op_sel:[0,0,1]
	v_mul_f32_e32 v169, 0x45000000, v171
	v_mfma_f32_16x16x32_fp8_fp8 v[156:159], v[0:1], v[94:95], v[156:159]
	v_mov_b32_e32 v1, v2
	v_cndmask_b32_e32 v169, 0, v169, vcc
	s_cmp_ge_i32 s52, s60
	v_mfma_f32_16x16x32_fp8_fp8 v[152:155], v[2:3], v[96:97], v[152:155]
	s_cselect_b64 s[38:39], -1, 0
	s_cmp_lt_i32 s52, s48
	s_cselect_b64 s[52:53], -1, 0
	v_mfma_f32_16x16x32_fp8_fp8 v[160:163], v[2:3], v[98:99], v[160:163]
	v_and_b32_e32 v2, v170, v249
	v_mov_b32_e32 v170, v0
	v_cvt_pk_fp8_f32 v170, v169, v169
	s_and_b64 vcc, s[38:39], s[52:53]
	v_mfma_f32_16x16x32_fp8_fp8 v[164:167], v[0:1], v[96:97], v[164:167]
	s_or_b32 s52, s30, 11
	v_cvt_pk_fp8_f32 v170, v169, v169 op_sel:[0,0,1]
	v_mul_f32_e32 v169, 0x45000000, v172
	v_mfma_f32_16x16x32_fp8_fp8 v[156:159], v[0:1], v[98:99], v[156:159]
	v_mov_b32_e32 v1, v2
	v_cndmask_b32_e32 v169, 0, v169, vcc
	s_cmp_ge_i32 s52, s60
	v_mfma_f32_16x16x32_fp8_fp8 v[152:155], v[2:3], v[100:101], v[152:155]
	s_cselect_b64 s[38:39], -1, 0
	s_cmp_lt_i32 s52, s48
	s_cselect_b64 s[52:53], -1, 0
	v_mfma_f32_16x16x32_fp8_fp8 v[160:163], v[2:3], v[102:103], v[160:163]
	v_and_b32_e32 v2, v170, v249
	v_mov_b32_e32 v170, v0
	v_cvt_pk_fp8_f32 v170, v169, v169
	s_and_b64 vcc, s[38:39], s[52:53]
	v_mfma_f32_16x16x32_fp8_fp8 v[164:167], v[0:1], v[100:101], v[164:167]
	s_or_b32 s52, s30, 12
	v_cvt_pk_fp8_f32 v170, v169, v169 op_sel:[0,0,1]
	v_mul_f32_e32 v169, 0x45000000, v173
	v_mfma_f32_16x16x32_fp8_fp8 v[156:159], v[0:1], v[102:103], v[156:159]
	v_mov_b32_e32 v1, v2
	v_cndmask_b32_e32 v169, 0, v169, vcc
	s_cmp_ge_i32 s52, s60
	v_mfma_f32_16x16x32_fp8_fp8 v[152:155], v[2:3], v[104:105], v[152:155]
	s_cselect_b64 s[38:39], -1, 0
	s_cmp_lt_i32 s52, s48
	s_cselect_b64 s[52:53], -1, 0
	v_mfma_f32_16x16x32_fp8_fp8 v[160:163], v[2:3], v[106:107], v[160:163]
	v_and_b32_e32 v2, v170, v249
	v_mov_b32_e32 v170, v0
	v_cvt_pk_fp8_f32 v170, v169, v169
	v_mfma_f32_16x16x32_fp8_fp8 v[164:167], v[0:1], v[104:105], v[164:167]
	s_and_b64 vcc, s[38:39], s[52:53]
	v_mov_b32_e32 v172, v0
	v_cvt_pk_fp8_f32 v170, v169, v169 op_sel:[0,0,1]
	v_mfma_f32_16x16x32_fp8_fp8 v[156:159], v[0:1], v[106:107], v[156:159]
	v_mov_b32_e32 v1, v2
	s_or_b32 s52, s30, 13
	s_cmp_ge_i32 s52, s60
	v_mfma_f32_16x16x32_fp8_fp8 v[152:155], v[2:3], v[108:109], v[152:155]
	s_cselect_b64 s[38:39], -1, 0
	s_cmp_lt_i32 s52, s48
	s_cselect_b64 s[52:53], -1, 0
	v_mfma_f32_16x16x32_fp8_fp8 v[160:163], v[2:3], v[110:111], v[160:163]
	v_and_b32_e32 v2, v170, v249
	ds_read_b128 v[168:171], v168 offset:48
	v_mov_b32_e32 v173, v0
	v_mfma_f32_16x16x32_fp8_fp8 v[164:167], v[0:1], v[108:109], v[164:167]
	s_waitcnt lgkmcnt(0)
	v_mul_f32_e32 v168, 0x45000000, v168
	v_cndmask_b32_e32 v168, 0, v168, vcc
	v_cvt_pk_fp8_f32 v172, v168, v168
	s_and_b64 vcc, s[38:39], s[52:53]
	v_mfma_f32_16x16x32_fp8_fp8 v[156:159], v[0:1], v[110:111], v[156:159]
	v_mov_b32_e32 v1, v2
	v_cvt_pk_fp8_f32 v172, v168, v168 op_sel:[0,0,1]
	v_mul_f32_e32 v168, 0x45000000, v169
	v_cndmask_b32_e32 v168, 0, v168, vcc
	v_mov_b32_e32 v169, v0
	v_cvt_pk_fp8_f32 v169, v168, v168
	v_mfma_f32_16x16x32_fp8_fp8 v[152:155], v[2:3], v[112:113], v[152:155]
	s_or_b32 s52, s30, 14
	s_cmp_ge_i32 s52, s60
	v_cvt_pk_fp8_f32 v169, v168, v168 op_sel:[0,0,1]
	v_mfma_f32_16x16x32_fp8_fp8 v[160:163], v[2:3], v[114:115], v[160:163]
	v_and_b32_e32 v2, v172, v249
	s_cselect_b64 s[38:39], -1, 0
	s_cmp_lt_i32 s52, s48
	s_cselect_b64 s[52:53], -1, 0
	v_mul_f32_e32 v168, 0x45000000, v170
	s_and_b64 vcc, s[38:39], s[52:53]
	v_mfma_f32_16x16x32_fp8_fp8 v[164:167], v[0:1], v[112:113], v[164:167]
	v_cndmask_b32_e32 v168, 0, v168, vcc
	s_or_b32 s30, s30, 15
	s_cmp_ge_i32 s30, s60
	v_mfma_f32_16x16x32_fp8_fp8 v[156:159], v[0:1], v[114:115], v[156:159]
	v_mov_b32_e32 v1, v2
	s_cselect_b64 s[38:39], -1, 0
	s_cmp_lt_i32 s30, s48
	v_mfma_f32_16x16x32_fp8_fp8 v[152:155], v[2:3], v[120:121], v[152:155]
	s_cselect_b64 s[52:53], -1, 0
	s_and_b64 vcc, s[38:39], s[52:53]
	s_add_i32 s30, s61, -1
	v_mfma_f32_16x16x32_fp8_fp8 v[160:163], v[2:3], v[122:123], v[160:163]
	v_and_b32_e32 v2, v169, v249
	v_mov_b32_e32 v169, v0
	v_cvt_pk_fp8_f32 v169, v168, v168
	v_mfma_f32_16x16x32_fp8_fp8 v[164:167], v[0:1], v[120:121], v[164:167]
	s_cmp_lg_u32 s56, s30
	v_cvt_pk_fp8_f32 v169, v168, v168 op_sel:[0,0,1]
	v_mul_f32_e32 v168, 0x45000000, v171
	v_mfma_f32_16x16x32_fp8_fp8 v[156:159], v[0:1], v[122:123], v[156:159]
	v_mov_b32_e32 v1, v2
	v_cndmask_b32_e32 v172, 0, v168, vcc
	v_cvt_pk_fp8_f32 v173, v172, v172
	v_mfma_f32_16x16x32_fp8_fp8 v[152:155], v[2:3], v[124:125], v[152:155]
	v_cvt_pk_fp8_f32 v173, v172, v172 op_sel:[0,0,1]
	v_mfma_f32_16x16x32_fp8_fp8 v[160:163], v[2:3], v[126:127], v[160:163]
	v_and_b32_e32 v2, v169, v249
	v_mfma_f32_16x16x32_fp8_fp8 v[164:167], v[0:1], v[124:125], v[164:167]
	v_mfma_f32_16x16x32_fp8_fp8 v[156:159], v[0:1], v[126:127], v[156:159]
	v_mov_b32_e32 v1, v2
	v_mfma_f32_16x16x32_fp8_fp8 v[152:155], v[2:3], v[144:145], v[152:155]
	v_mfma_f32_16x16x32_fp8_fp8 v[168:171], v[2:3], v[146:147], v[160:163]
	v_and_b32_e32 v2, v173, v249
	v_mfma_f32_16x16x32_fp8_fp8 v[164:167], v[0:1], v[144:145], v[164:167]
	v_mfma_f32_16x16x32_fp8_fp8 v[156:159], v[0:1], v[146:147], v[156:159]
	v_mov_b32_e32 v1, v2
	s_nop 0
	v_mfma_f32_16x16x32_fp8_fp8 v[160:163], v[2:3], v[148:149], v[152:155]
	v_mfma_f32_16x16x32_fp8_fp8 v[164:167], v[0:1], v[148:149], v[164:167]
	v_mfma_f32_16x16x32_fp8_fp8 v[152:155], v[2:3], v[150:151], v[168:171]
	v_mfma_f32_16x16x32_fp8_fp8 v[156:159], v[0:1], v[150:151], v[156:159]
	s_cbranch_scc1 .LBB0_1816
; __device__ __forceinline__ void peer_token_end(Frame& F, const Args& a, int layer, bool last, bool final_half, size_t tok, int lane, const f32x2 (&out)[8], const f32x4 (&hpre)[4], const v4u (&gpre)[2], const v4u& p8pre) {
;     ...
;     for (int i = 0; i < 4; ++i) { const f32x2 lo = __builtin_amdgcn_cvt_pk_f32_fp8((int)p8pre[i], false), hi = __builtin_amdgcn_cvt_pk_f32_fp8((int)p8pre[i], true);
;         pe[i] = (f32x4){lo.x, lo.y, hi.x, hi.y} * (1.f / 256.f) + (f32x4){out[2 * i].x, out[2 * i].y, out[2 * i + 1].x, out[2 * i + 1].y}; }
;     if (!final_half) {
;         v4u w;
; #pragma unroll
;         for (int i = 0; i < 4; ++i) { const f32x4 s8 = pe[i] * 256.f; int t = 0; t = __builtin_amdgcn_cvt_pk_fp8_f32(s8.x, s8.y, t, false); t = __builtin_amdgcn_cvt_pk_fp8_f32(s8.z, s8.w, t, true); w[i] = (unsigned)t; }
;         *(v4u*)((unsigned char*)(F.ws + WS_P8) + tok * 1024 + 16 * lane) = w;
	v_cvt_pk_f32_fp8_e32 v[2:3], v140
	v_cvt_pk_f32_fp8_e32 v[170:171], v141
	v_cvt_pk_f32_fp8_sdwa v[172:173], v141 src0_sel:WORD_1
	v_cvt_pk_f32_fp8_sdwa v[188:189], v142 src0_sel:WORD_1
	v_pk_mul_f32 v[2:3], v[2:3], s[12:13] op_sel_hi:[1,0]
	v_cvt_pk_f32_fp8_e32 v[186:187], v142
	v_pk_fma_f32 v[174:175], v[160:161], s[14:15], v[2:3] op_sel_hi:[1,0,1]
	v_pk_mul_f32 v[2:3], v[170:171], s[12:13] op_sel_hi:[1,0]
	v_pk_mul_f32 v[170:171], v[172:173], s[12:13] op_sel_hi:[1,0]
	v_cvt_pk_f32_fp8_sdwa v[168:169], v140 src0_sel:WORD_1
	v_pk_fma_f32 v[172:173], v[166:167], s[14:15], v[170:171] op_sel_hi:[1,0,1]
	v_pk_mul_f32 v[170:171], v[188:189], s[12:13] op_sel_hi:[1,0]
	v_cvt_pk_f32_fp8_e32 v[188:189], v143
	v_cvt_pk_f32_fp8_sdwa v[192:193], v143 src0_sel:WORD_1
	s_ashr_i32 s30, s58, 31
	s_add_u32 s52, s0, s58
	v_pk_fma_f32 v[184:185], v[164:165], s[14:15], v[2:3] op_sel_hi:[1,0,1]
	v_pk_mul_f32 v[2:3], v[186:187], s[12:13] op_sel_hi:[1,0]
	s_addc_u32 s53, s1, s30
	v_pk_mul_f32 v[168:169], v[168:169], s[12:13] op_sel_hi:[1,0]
	v_pk_fma_f32 v[186:187], v[154:155], s[14:15], v[170:171] op_sel_hi:[1,0,1]
	v_pk_fma_f32 v[190:191], v[152:153], s[14:15], v[2:3] op_sel_hi:[1,0,1]
	v_pk_mul_f32 v[2:3], v[188:189], s[12:13] op_sel_hi:[1,0]
	v_pk_mul_f32 v[170:171], v[192:193], s[12:13] op_sel_hi:[1,0]
	s_lshl_b64 s[38:39], s[52:53], 10
	v_pk_fma_f32 v[168:169], v[162:163], s[14:15], v[168:169] op_sel_hi:[1,0,1]
	v_pk_fma_f32 v[188:189], v[158:159], s[14:15], v[170:171] op_sel_hi:[1,0,1]
	v_pk_fma_f32 v[192:193], v[156:157], s[14:15], v[2:3] op_sel_hi:[1,0,1]
	s_andn2_b64 vcc, exec, s[46:47]
	s_mov_b64 s[54:55], -1
	s_cbranch_vccnz .LBB0_1811
	v_pk_mul_f32 v[2:3], v[174:175], s[8:9] op_sel_hi:[1,0]
	v_mov_b32_e32 v194, v0
	v_cvt_pk_fp8_f32 v194, v2, v3
	v_pk_mul_f32 v[2:3], v[184:185], s[8:9] op_sel_hi:[1,0]
	v_mov_b32_e32 v195, v0
	v_cvt_pk_fp8_f32 v195, v2, v3
	v_pk_mul_f32 v[2:3], v[168:169], s[8:9] op_sel_hi:[1,0]
	v_mov_b32_e32 v196, v0
	v_cvt_pk_fp8_f32 v194, v2, v3 op_sel:[0,0,1]
	v_pk_mul_f32 v[2:3], v[172:173], s[8:9] op_sel_hi:[1,0]
	v_mov_b32_e32 v197, v0
	v_cvt_pk_fp8_f32 v195, v2, v3 op_sel:[0,0,1]
	v_pk_mul_f32 v[2:3], v[190:191], s[8:9] op_sel_hi:[1,0]
	s_mov_b64 s[54:55], 0
	v_cvt_pk_fp8_f32 v196, v2, v3
	v_pk_mul_f32 v[2:3], v[192:193], s[8:9] op_sel_hi:[1,0]
	s_nop 0
	v_cvt_pk_fp8_f32 v197, v2, v3
	v_pk_mul_f32 v[2:3], v[186:187], s[8:9] op_sel_hi:[1,0]
	s_nop 0
	v_cvt_pk_fp8_f32 v196, v2, v3 op_sel:[0,0,1]
	v_pk_mul_f32 v[2:3], v[188:189], s[8:9] op_sel_hi:[1,0]
	s_nop 0
	v_cvt_pk_fp8_f32 v197, v2, v3 op_sel:[0,0,1]
	v_lshl_add_u64 v[2:3], v[234:235], 0, s[38:39]
	global_store_dwordx4 v[2:3], v[194:197], off
